# k_agg1 prologue: W2 slice values no longer waited/masked before the first chunk (masking moved to the LDS fill after chunk 0)
# speedup vs baseline: 1.0025x; 1.0025x over previous
_Z6k_agg1PKDF16_PK15HIP_vector_typeIiLj2EEPKtPKfS8_S8_Pf:
	s_and_b32 s8, s2, 3
	s_lshl_b32 s3, s8, 6
	s_movk_i32 s34, 0x80
	v_add_u32_e32 v6, 0x140, v0
	s_load_dwordx4 s[4:7], s[0:1], 0x20
	s_load_dwordx2 s[28:29], s[0:1], 0x30
	v_and_b32_e32 v1, 7, v0
	v_and_or_b32 v4, v0, 56, s3
	v_lshrrev_b32_e32 v2, 6, v0
	v_lshrrev_b32_e32 v10, 6, v6
	v_cmp_eq_u32_e64 s[18:19], 7, v1
	v_or_b32_e32 v5, v2, v4
	v_and_or_b32 v4, v10, 7, v4
	v_cndmask_b32_e64 v3, v1, 0, s[18:19]
	v_mul_u32_u24_e32 v5, 7, v5
	v_mul_u32_u24_e32 v4, 7, v4
	v_add_lshl_u32 v5, v5, v3, 2
	v_add_lshl_u32 v3, v4, v3, 2
	s_waitcnt lgkmcnt(0)
	global_load_dword v26, v5, s[6:7]
	global_load_dword v27, v3, s[6:7]
	v_and_b32_e32 v3, 63, v0
	v_or_b32_e32 v3, s3, v3
	v_lshlrev_b32_e32 v3, 2, v3
	global_load_dword v20, v3, s[4:5]
	s_load_dwordx8 s[20:27], s[0:1], 0x0
	s_lshr_b32 s6, s2, 2
	v_lshlrev_b32_e32 v3, 2, v0
	s_movk_i32 s30, 0xe0
	s_movk_i32 s3, 0x200
	s_movk_i32 s4, 0xc0
	s_mul_i32 s31, s8, 0x61a880
	v_mad_u64_u32 v[8:9], s[6:7], s6, 5, v[2:3]
	v_lshlrev_b32_e32 v4, 2, v1
	v_mov_b32_e32 v5, 0
	v_bfe_u32 v21, v0, 3, 3
	v_cmp_gt_u32_e32 vcc, 64, v0
	v_cmp_gt_u32_e64 s[0:1], s3, v0
	v_cmp_gt_u32_e64 s[2:3], s4, v0
	v_cmp_ne_u32_e64 s[4:5], 7, v1
	v_lshlrev_b32_e32 v6, 4, v1
	v_lshlrev_b32_e32 v22, 5, v1
	v_mul_u32_u24_e32 v0, 28, v1
	v_cmp_eq_u32_e64 s[6:7], 1, v1
	v_cmp_eq_u32_e64 s[8:9], 2, v1
	v_cmp_eq_u32_e64 s[10:11], 3, v1
	v_cmp_eq_u32_e64 s[12:13], 4, v1
	v_cmp_eq_u32_e64 s[14:15], 5, v1
	v_cmp_eq_u32_e64 s[16:17], 6, v1
	v_and_or_b32 v1, v3, s30, v4
	s_waitcnt lgkmcnt(0)
	s_add_u32 s20, s20, s31
	s_mov_b32 s33, 0
	v_or_b32_e32 v9, 0x800, v3
	v_mov_b32_e32 v7, v6
	v_add_u32_e32 v23, v4, v0
	v_lshl_or_b32 v24, v2, 8, v1
	v_lshl_or_b32 v25, v10, 8, v1
	v_lshl_add_u64 v[10:11], s[28:29], 0, v[4:5]
	s_addc_u32 s21, s21, 0
	v_mov_b32_e32 v28, 7
	s_branch .LBB3_2

.LBB3_14:
	v_cndmask_b32_e64 v26, 0, v26, s[4:5]
	ds_write_b32 v24, v26
	s_or_b64 exec, exec, s[18:19]
	s_and_saveexec_b64 s[18:19], s[2:3]
	s_cbranch_execz .LBB3_9
.LBB3_15:
	v_cndmask_b32_e64 v27, 0, v27, s[4:5]
	ds_write_b32 v25, v27
	s_or_b64 exec, exec, s[18:19]
	s_and_saveexec_b64 s[18:19], vcc
	s_cbranch_execnz .LBB3_10
	s_branch .LBB3_11
